# sel-attn bias-table reads: one base address + ds_read2 offsets (7 fewer VALU per quad-tile)
# baseline (speedup 1.0000x reference)
; #define LAS __attribute__((address_space(3)))
;     ...
;                 if (MODE == 3) { tokmask = (unsigned)__ballot(lane < TW && ((selm[(wave * TW + (lane & (TW - 1))) * 8 + (jblk >> 5)] >> (jblk & 31)) & 1u)); if (tokmask == 0u) continue; }
; #pragma unroll
;                 for (int qd = 0; qd < NQ; ++qd) {
;                     const int tq = tw0 + 4 * qd + (n >> 2);
;                     if (DBG == 3) continue;
;                     bool colsel = true;
;                     if (MODE == 3) { colsel = (tokmask >> (4 * qd + (n >> 2))) & 1u; if (((tokmask >> (4 * qd)) & 0xfu) == 0u) continue; }
;                     {
;                         f32x4 sc[4];
;                         float bia[4][4];
;                         bf16x8 akq[4][2], avq[2][4];
;                         if (MODE == 3) {
; #pragma unroll
;                             for (int kt = 0; kt < 4; ++kt)
; #pragma unroll
;                                 for (int ks = 0; ks < 2; ++ks) akq[kt][ks] = *(const LAS bf16x8*)(L + LK + (16 * kt + n) * 128 + ((((4 * ks + q) ^ n) & 7) << 4));
;                             if (!far) { const LAS float* tp = biasd + hr * NT + (DOFF - tq + p0) + 4 * q;
; #pragma unroll
;                                 for (int kt = 0; kt < 4; ++kt)
; #pragma unroll
;                                     for (int r = 0; r < 4; ++r) bia[kt][r] = tp[16 * kt + r]; }
.LBB0_1153:
	v_mbcnt_lo_u32_b32 v106, -1, 0
	v_mbcnt_hi_u32_b32 v106, -1, v106
	s_add_i32 s0, s55, -13
	v_lshrrev_b32_e32 v107, 3, v106
	v_add_u32_e32 v107, s0, v107
	s_add_i32 s0, 0, 0x25080
	v_min_i32_e32 v107, s52, v107
	v_lshl_add_u32 v107, v107, 2, s0
	ds_read_b32 v107, v107
	s_waitcnt lgkmcnt(0)
	v_lshrrev_b32_e32 v106, 5, v107
	v_lshl_add_u32 v106, v106, 2, v157
	ds_read_b32 v106, v106
	s_waitcnt lgkmcnt(0)
	v_lshrrev_b32_e32 v106, v107, v106
	v_and_b32_e32 v106, 1, v106
	v_cmp_eq_u32_e64 s[90:91], 1, v106
	s_cmp_lt_i32 s67, 0
	s_cselect_b64 s[0:1], -1, 0
	s_cmp_gt_i32 s67, s15
	s_cselect_b64 s[2:3], -1, 0
	s_or_b64 s[0:1], s[0:1], s[2:3]
	s_and_b64 vcc, exec, s[0:1]
	s_waitcnt lgkmcnt(0)
	s_barrier
	s_cbranch_vccnz .LBB0_1175
	s_bfe_u32 s0, s90, 0x80000
	s_cmp_eq_u32 s0, 0
	s_cbranch_scc1 .LBB0_1175
	s_sub_i32 s1, s16, s67
	s_cmpk_lt_i32 s1, 0x316
	s_cselect_b64 s[2:3], -1, 0
	v_cndmask_b32_e64 v106, 0, 1, s[2:3]
	s_and_b32 s1, s0, 15
	s_cmp_eq_u32 s1, 0
	v_cmp_ne_u32_e64 s[2:3], 1, v106
	s_cbranch_scc1 .LBB0_1166
	v_add_u32_e32 v238, v187, v195
	v_add_u32_e32 v237, v187, v204
	ds_read_b128 v[106:109], v238
	ds_read_b128 v[110:113], v238 offset:2048
	ds_read_b128 v[126:129], v237
	ds_read_b128 v[114:117], v237 offset:2048
	ds_read_b128 v[118:121], v238 offset:4096
	ds_read_b128 v[122:125], v238 offset:6144
	ds_read_b128 v[134:137], v237 offset:4096
	ds_read_b128 v[130:133], v237 offset:6144
	s_and_b64 vcc, exec, s[2:3]
	s_cbranch_vccnz .LBB0_1160
	v_sub_u32_e32 v138, s67, v196
	v_lshl_add_u32 v138, v138, 2, v233
	v_add_u32_e32 v139, 0xffc, v138
	ds_read2_b32 v[168:169], v139 offset1:1
	ds_read2_b32 v[170:171], v139 offset0:2 offset1:3
	ds_read2_b32 v[172:173], v139 offset0:16 offset1:17
	ds_read2_b32 v[174:175], v139 offset0:18 offset1:19
	ds_read2_b32 v[176:177], v139 offset0:32 offset1:33
	ds_read2_b32 v[178:179], v139 offset0:34 offset1:35
	ds_read2_b32 v[180:181], v139 offset0:48 offset1:49
	ds_read2_b32 v[182:183], v139 offset0:50 offset1:51

; #define LAS __attribute__((address_space(3)))
;     ...
;                     if (MODE == 3) { colsel = (tokmask >> (4 * qd + (n >> 2))) & 1u; if (((tokmask >> (4 * qd)) & 0xfu) == 0u) continue; }
;                     {
;                         f32x4 sc[4];
;                         float bia[4][4];
;                         bf16x8 akq[4][2], avq[2][4];
;                         if (MODE == 3) {
; #pragma unroll
;                             for (int kt = 0; kt < 4; ++kt)
; #pragma unroll
;                                 for (int ks = 0; ks < 2; ++ks) akq[kt][ks] = *(const LAS bf16x8*)(L + LK + (16 * kt + n) * 128 + ((((4 * ks + q) ^ n) & 7) << 4));
;                             if (!far) { const LAS float* tp = biasd + hr * NT + (DOFF - tq + p0) + 4 * q;
; #pragma unroll
;                                 for (int kt = 0; kt < 4; ++kt)
; #pragma unroll
;                                     for (int r = 0; r < 4; ++r) bia[kt][r] = tp[16 * kt + r]; }
.LBB0_1166:
	s_and_b32 s1, s0, 0xf0
	s_cmp_eq_u32 s1, 0
	s_cbranch_scc1 .LBB0_1175
	v_add_u32_e32 v238, v187, v195
	v_add_u32_e32 v237, v187, v204
	ds_read_b128 v[106:109], v238
	ds_read_b128 v[110:113], v238 offset:2048
	ds_read_b128 v[126:129], v237
	ds_read_b128 v[114:117], v237 offset:2048
	ds_read_b128 v[118:121], v238 offset:4096
	ds_read_b128 v[122:125], v238 offset:6144
	ds_read_b128 v[134:137], v237 offset:4096
	ds_read_b128 v[130:133], v237 offset:6144
	s_and_b64 vcc, exec, s[2:3]
	s_cbranch_vccnz .LBB0_1169
	v_sub_u32_e32 v138, s67, v184
	v_lshl_add_u32 v138, v138, 2, v233
	v_add_u32_e32 v139, 0xffc, v138
	ds_read2_b32 v[168:169], v139 offset1:1
	ds_read2_b32 v[170:171], v139 offset0:2 offset1:3
	ds_read2_b32 v[172:173], v139 offset0:16 offset1:17
	ds_read2_b32 v[174:175], v139 offset0:18 offset1:19
	ds_read2_b32 v[176:177], v139 offset0:32 offset1:33
	ds_read2_b32 v[178:179], v139 offset0:34 offset1:35
	ds_read2_b32 v[180:181], v139 offset0:48 offset1:49
	ds_read2_b32 v[182:183], v139 offset0:50 offset1:51

; #define LAS __attribute__((address_space(3)))
;     ...
;                     if (MODE == 3) { colsel = (tokmask >> (4 * qd + (n >> 2))) & 1u; if (((tokmask >> (4 * qd)) & 0xfu) == 0u) continue; }
;                     {
;                         f32x4 sc[4];
;                         float bia[4][4];
;                         bf16x8 akq[4][2], avq[2][4];
;                         if (MODE == 3) {
; #pragma unroll
;                             for (int kt = 0; kt < 4; ++kt)
; #pragma unroll
;                                 for (int ks = 0; ks < 2; ++ks) akq[kt][ks] = *(const LAS bf16x8*)(L + LK + (16 * kt + n) * 128 + ((((4 * ks + q) ^ n) & 7) << 4));
;                             if (!far) { const LAS float* tp = biasd + hr * NT + (DOFF - tq + p0) + 4 * q;
; #pragma unroll
;                                 for (int kt = 0; kt < 4; ++kt)
; #pragma unroll
;                                     for (int r = 0; r < 4; ++r) bia[kt][r] = tp[16 * kt + r]; }
.LBB0_1175:
	s_cmp_lt_i32 s66, 0
	s_cselect_b64 s[0:1], -1, 0
	s_cmp_gt_i32 s66, s15
	s_cselect_b64 s[2:3], -1, 0
	s_or_b64 s[0:1], s[0:1], s[2:3]
	s_and_b64 vcc, exec, s[0:1]
	s_cbranch_vccnz .LBB0_1197
	s_bfe_u32 s0, s90, 0x80008
	s_cmp_eq_u32 s0, 0
	s_cbranch_scc1 .LBB0_1197
	s_sub_i32 s1, s16, s66
	s_cmpk_lt_i32 s1, 0x316
	s_cselect_b64 s[2:3], -1, 0
	v_cndmask_b32_e64 v106, 0, 1, s[2:3]
	s_and_b32 s1, s0, 15
	s_cmp_eq_u32 s1, 0
	v_cmp_ne_u32_e64 s[2:3], 1, v106
	s_cbranch_scc1 .LBB0_1188
	v_add_u32_e32 v238, v187, v195
	v_add_u32_e32 v237, v187, v204
	ds_read_b128 v[106:109], v238 offset:16384
	ds_read_b128 v[110:113], v238 offset:18432
	ds_read_b128 v[126:129], v237 offset:16384
	ds_read_b128 v[114:117], v237 offset:18432
	ds_read_b128 v[118:121], v238 offset:20480
	ds_read_b128 v[122:125], v238 offset:22528
	ds_read_b128 v[134:137], v237 offset:20480
	ds_read_b128 v[130:133], v237 offset:22528
	s_and_b64 vcc, exec, s[2:3]
	s_cbranch_vccnz .LBB0_1182
	v_sub_u32_e32 v138, s66, v196
	v_lshl_add_u32 v138, v138, 2, v233
	v_add_u32_e32 v139, 0xffc, v138
	ds_read2_b32 v[168:169], v139 offset1:1
	ds_read2_b32 v[170:171], v139 offset0:2 offset1:3
	ds_read2_b32 v[172:173], v139 offset0:16 offset1:17
	ds_read2_b32 v[174:175], v139 offset0:18 offset1:19
	ds_read2_b32 v[176:177], v139 offset0:32 offset1:33
	ds_read2_b32 v[178:179], v139 offset0:34 offset1:35
	ds_read2_b32 v[180:181], v139 offset0:48 offset1:49
	ds_read2_b32 v[182:183], v139 offset0:50 offset1:51

; #define LAS __attribute__((address_space(3)))
;     ...
;                     if (MODE == 3) { colsel = (tokmask >> (4 * qd + (n >> 2))) & 1u; if (((tokmask >> (4 * qd)) & 0xfu) == 0u) continue; }
;                     {
;                         f32x4 sc[4];
;                         float bia[4][4];
;                         bf16x8 akq[4][2], avq[2][4];
;                         if (MODE == 3) {
; #pragma unroll
;                             for (int kt = 0; kt < 4; ++kt)
; #pragma unroll
;                                 for (int ks = 0; ks < 2; ++ks) akq[kt][ks] = *(const LAS bf16x8*)(L + LK + (16 * kt + n) * 128 + ((((4 * ks + q) ^ n) & 7) << 4));
;                             if (!far) { const LAS float* tp = biasd + hr * NT + (DOFF - tq + p0) + 4 * q;
; #pragma unroll
;                                 for (int kt = 0; kt < 4; ++kt)
; #pragma unroll
;                                     for (int r = 0; r < 4; ++r) bia[kt][r] = tp[16 * kt + r]; }
.LBB0_1188:
	s_and_b32 s1, s0, 0xf0
	s_cmp_eq_u32 s1, 0
	s_cbranch_scc1 .LBB0_1197
	v_add_u32_e32 v238, v187, v195
	v_add_u32_e32 v237, v187, v204
	ds_read_b128 v[106:109], v238 offset:16384
	ds_read_b128 v[110:113], v238 offset:18432
	ds_read_b128 v[126:129], v237 offset:16384
	ds_read_b128 v[114:117], v237 offset:18432
	ds_read_b128 v[118:121], v238 offset:20480
	ds_read_b128 v[122:125], v238 offset:22528
	ds_read_b128 v[134:137], v237 offset:20480
	ds_read_b128 v[130:133], v237 offset:22528
	s_and_b64 vcc, exec, s[2:3]
	s_cbranch_vccnz .LBB0_1191
	v_sub_u32_e32 v138, s66, v184
	v_lshl_add_u32 v138, v138, 2, v233
	v_add_u32_e32 v139, 0xffc, v138
	ds_read2_b32 v[168:169], v139 offset1:1
	ds_read2_b32 v[170:171], v139 offset0:2 offset1:3
	ds_read2_b32 v[172:173], v139 offset0:16 offset1:17
	ds_read2_b32 v[174:175], v139 offset0:18 offset1:19
	ds_read2_b32 v[176:177], v139 offset0:32 offset1:33
	ds_read2_b32 v[178:179], v139 offset0:34 offset1:35
	ds_read2_b32 v[180:181], v139 offset0:48 offset1:49
	ds_read2_b32 v[182:183], v139 offset0:50 offset1:51

; #define LAS __attribute__((address_space(3)))
;     ...
;                     if (MODE == 3) { colsel = (tokmask >> (4 * qd + (n >> 2))) & 1u; if (((tokmask >> (4 * qd)) & 0xfu) == 0u) continue; }
;                     {
;                         f32x4 sc[4];
;                         float bia[4][4];
;                         bf16x8 akq[4][2], avq[2][4];
;                         if (MODE == 3) {
; #pragma unroll
;                             for (int kt = 0; kt < 4; ++kt)
; #pragma unroll
;                                 for (int ks = 0; ks < 2; ++ks) akq[kt][ks] = *(const LAS bf16x8*)(L + LK + (16 * kt + n) * 128 + ((((4 * ks + q) ^ n) & 7) << 4));
;                             if (!far) { const LAS float* tp = biasd + hr * NT + (DOFF - tq + p0) + 4 * q;
; #pragma unroll
;                                 for (int kt = 0; kt < 4; ++kt)
; #pragma unroll
;                                     for (int r = 0; r < 4; ++r) bia[kt][r] = tp[16 * kt + r]; }
.LBB0_1197:
	s_cmp_lt_i32 s65, 0
	s_cselect_b64 s[0:1], -1, 0
	s_cmp_gt_i32 s65, s15
	s_cselect_b64 s[2:3], -1, 0
	s_or_b64 s[0:1], s[0:1], s[2:3]
	s_and_b64 vcc, exec, s[0:1]
	s_cbranch_vccnz .LBB0_1219
	s_bfe_u32 s0, s90, 0x80010
	s_cmp_eq_u32 s0, 0
	s_cbranch_scc1 .LBB0_1219
	s_sub_i32 s1, s16, s65
	s_cmpk_lt_i32 s1, 0x316
	s_cselect_b64 s[2:3], -1, 0
	v_cndmask_b32_e64 v106, 0, 1, s[2:3]
	s_and_b32 s1, s0, 15
	s_cmp_eq_u32 s1, 0
	v_cmp_ne_u32_e64 s[2:3], 1, v106
	s_cbranch_scc1 .LBB0_1210
	v_add_u32_e32 v238, v187, v195
	v_add_u32_e32 v237, v187, v204
	ds_read_b128 v[106:109], v238 offset:32768
	ds_read_b128 v[110:113], v238 offset:34816
	ds_read_b128 v[126:129], v237 offset:32768
	ds_read_b128 v[114:117], v237 offset:34816
	ds_read_b128 v[118:121], v238 offset:36864
	ds_read_b128 v[122:125], v238 offset:38912
	ds_read_b128 v[134:137], v237 offset:36864
	ds_read_b128 v[130:133], v237 offset:38912
	s_and_b64 vcc, exec, s[2:3]
	s_cbranch_vccnz .LBB0_1204
	v_sub_u32_e32 v138, s65, v196
	v_lshl_add_u32 v138, v138, 2, v233
	v_add_u32_e32 v139, 0xffc, v138
	ds_read2_b32 v[168:169], v139 offset1:1
	ds_read2_b32 v[170:171], v139 offset0:2 offset1:3
	ds_read2_b32 v[172:173], v139 offset0:16 offset1:17
	ds_read2_b32 v[174:175], v139 offset0:18 offset1:19
	ds_read2_b32 v[176:177], v139 offset0:32 offset1:33
	ds_read2_b32 v[178:179], v139 offset0:34 offset1:35
	ds_read2_b32 v[180:181], v139 offset0:48 offset1:49
	ds_read2_b32 v[182:183], v139 offset0:50 offset1:51

; #define LAS __attribute__((address_space(3)))
;     ...
;                     if (MODE == 3) { colsel = (tokmask >> (4 * qd + (n >> 2))) & 1u; if (((tokmask >> (4 * qd)) & 0xfu) == 0u) continue; }
;                     {
;                         f32x4 sc[4];
;                         float bia[4][4];
;                         bf16x8 akq[4][2], avq[2][4];
;                         if (MODE == 3) {
; #pragma unroll
;                             for (int kt = 0; kt < 4; ++kt)
; #pragma unroll
;                                 for (int ks = 0; ks < 2; ++ks) akq[kt][ks] = *(const LAS bf16x8*)(L + LK + (16 * kt + n) * 128 + ((((4 * ks + q) ^ n) & 7) << 4));
;                             if (!far) { const LAS float* tp = biasd + hr * NT + (DOFF - tq + p0) + 4 * q;
; #pragma unroll
;                                 for (int kt = 0; kt < 4; ++kt)
; #pragma unroll
;                                     for (int r = 0; r < 4; ++r) bia[kt][r] = tp[16 * kt + r]; }
.LBB0_1210:
	s_and_b32 s1, s0, 0xf0
	s_cmp_eq_u32 s1, 0
	s_cbranch_scc1 .LBB0_1219
	v_add_u32_e32 v238, v187, v195
	v_add_u32_e32 v237, v187, v204
	ds_read_b128 v[106:109], v238 offset:32768
	ds_read_b128 v[110:113], v238 offset:34816
	ds_read_b128 v[126:129], v237 offset:32768
	ds_read_b128 v[114:117], v237 offset:34816
	ds_read_b128 v[118:121], v238 offset:36864
	ds_read_b128 v[122:125], v238 offset:38912
	ds_read_b128 v[134:137], v237 offset:36864
	ds_read_b128 v[130:133], v237 offset:38912
	s_and_b64 vcc, exec, s[2:3]
	s_cbranch_vccnz .LBB0_1213
	v_sub_u32_e32 v138, s65, v184
	v_lshl_add_u32 v138, v138, 2, v233
	v_add_u32_e32 v139, 0xffc, v138
	ds_read2_b32 v[168:169], v139 offset1:1
	ds_read2_b32 v[170:171], v139 offset0:2 offset1:3
	ds_read2_b32 v[172:173], v139 offset0:16 offset1:17
	ds_read2_b32 v[174:175], v139 offset0:18 offset1:19
	ds_read2_b32 v[176:177], v139 offset0:32 offset1:33
	ds_read2_b32 v[178:179], v139 offset0:34 offset1:35
	ds_read2_b32 v[180:181], v139 offset0:48 offset1:49
	ds_read2_b32 v[182:183], v139 offset0:50 offset1:51

; #define LAS __attribute__((address_space(3)))
;     ...
;                     if (MODE == 3) { colsel = (tokmask >> (4 * qd + (n >> 2))) & 1u; if (((tokmask >> (4 * qd)) & 0xfu) == 0u) continue; }
;                     {
;                         f32x4 sc[4];
;                         float bia[4][4];
;                         bf16x8 akq[4][2], avq[2][4];
;                         if (MODE == 3) {
; #pragma unroll
;                             for (int kt = 0; kt < 4; ++kt)
; #pragma unroll
;                                 for (int ks = 0; ks < 2; ++ks) akq[kt][ks] = *(const LAS bf16x8*)(L + LK + (16 * kt + n) * 128 + ((((4 * ks + q) ^ n) & 7) << 4));
;                             if (!far) { const LAS float* tp = biasd + hr * NT + (DOFF - tq + p0) + 4 * q;
; #pragma unroll
;                                 for (int kt = 0; kt < 4; ++kt)
; #pragma unroll
;                                     for (int r = 0; r < 4; ++r) bia[kt][r] = tp[16 * kt + r]; }
.LBB0_1219:
	s_cmp_lt_i32 s64, 0
	s_cselect_b64 s[0:1], -1, 0
	s_cmp_gt_i32 s64, s15
	s_cselect_b64 s[2:3], -1, 0
	s_or_b64 s[0:1], s[0:1], s[2:3]
	s_and_b64 vcc, exec, s[0:1]
	s_cbranch_vccnz .LBB0_1241
	s_bfe_u32 s0, s90, 0x80018
	s_cmp_eq_u32 s0, 0
	s_cbranch_scc1 .LBB0_1241
	s_sub_i32 s1, s16, s64
	s_cmpk_lt_i32 s1, 0x316
	s_cselect_b64 s[2:3], -1, 0
	s_and_b32 s1, s0, 15
	v_cndmask_b32_e64 v106, 0, 1, s[2:3]
	s_cmp_eq_u32 s1, 0
	v_add_u32_e32 v238, v187, v195
	v_add_u32_e32 v237, v187, v204
	v_cmp_ne_u32_e64 s[2:3], 1, v106
	s_cbranch_scc1 .LBB0_1232
	ds_read_b128 v[106:109], v238 offset:49152
	ds_read_b128 v[110:113], v238 offset:51200
	ds_read_b128 v[126:129], v237 offset:49152
	ds_read_b128 v[114:117], v237 offset:51200
	ds_read_b128 v[118:121], v238 offset:53248
	ds_read_b128 v[122:125], v238 offset:55296
	ds_read_b128 v[134:137], v237 offset:53248
	ds_read_b128 v[130:133], v237 offset:55296
	s_and_b64 vcc, exec, s[2:3]
	s_cbranch_vccnz .LBB0_1226
	v_sub_u32_e32 v138, s64, v196
	v_lshl_add_u32 v138, v138, 2, v233
	v_add_u32_e32 v139, 0xffc, v138
	ds_read2_b32 v[168:169], v139 offset1:1
	ds_read2_b32 v[170:171], v139 offset0:2 offset1:3
	ds_read2_b32 v[172:173], v139 offset0:16 offset1:17
	ds_read2_b32 v[174:175], v139 offset0:18 offset1:19
	ds_read2_b32 v[176:177], v139 offset0:32 offset1:33
	ds_read2_b32 v[178:179], v139 offset0:34 offset1:35
	ds_read2_b32 v[180:181], v139 offset0:48 offset1:49
	ds_read2_b32 v[182:183], v139 offset0:50 offset1:51

; #define LAS __attribute__((address_space(3)))
;     ...
;                     if (MODE == 3) { colsel = (tokmask >> (4 * qd + (n >> 2))) & 1u; if (((tokmask >> (4 * qd)) & 0xfu) == 0u) continue; }
;                     {
;                         f32x4 sc[4];
;                         float bia[4][4];
;                         bf16x8 akq[4][2], avq[2][4];
;                         if (MODE == 3) {
; #pragma unroll
;                             for (int kt = 0; kt < 4; ++kt)
; #pragma unroll
;                                 for (int ks = 0; ks < 2; ++ks) akq[kt][ks] = *(const LAS bf16x8*)(L + LK + (16 * kt + n) * 128 + ((((4 * ks + q) ^ n) & 7) << 4));
;                             if (!far) { const LAS float* tp = biasd + hr * NT + (DOFF - tq + p0) + 4 * q;
; #pragma unroll
;                                 for (int kt = 0; kt < 4; ++kt)
; #pragma unroll
;                                     for (int r = 0; r < 4; ++r) bia[kt][r] = tp[16 * kt + r]; }
.LBB0_1232:
	s_and_b32 s1, s0, 0xf0
	s_cmp_eq_u32 s1, 0
	s_cbranch_scc1 .LBB0_1241
	ds_read_b128 v[106:109], v238 offset:49152
	ds_read_b128 v[110:113], v238 offset:51200
	ds_read_b128 v[126:129], v237 offset:49152
	ds_read_b128 v[114:117], v237 offset:51200
	ds_read_b128 v[118:121], v238 offset:53248
	ds_read_b128 v[122:125], v238 offset:55296
	ds_read_b128 v[134:137], v237 offset:53248
	ds_read_b128 v[130:133], v237 offset:55296
	s_and_b64 vcc, exec, s[2:3]
	s_cbranch_vccnz .LBB0_1235
	v_sub_u32_e32 v138, s64, v184
	v_lshl_add_u32 v138, v138, 2, v233
	v_add_u32_e32 v139, 0xffc, v138
	ds_read2_b32 v[168:169], v139 offset1:1
	ds_read2_b32 v[170:171], v139 offset0:2 offset1:3
	ds_read2_b32 v[172:173], v139 offset0:16 offset1:17
	ds_read2_b32 v[174:175], v139 offset0:18 offset1:19
	ds_read2_b32 v[176:177], v139 offset0:32 offset1:33
	ds_read2_b32 v[178:179], v139 offset0:34 offset1:35
	ds_read2_b32 v[180:181], v139 offset0:48 offset1:49
	ds_read2_b32 v[182:183], v139 offset0:50 offset1:51

; #define LAS __attribute__((address_space(3)))
;     ...
;                     if (MODE == 3) { colsel = (tokmask >> (4 * qd + (n >> 2))) & 1u; if (((tokmask >> (4 * qd)) & 0xfu) == 0u) continue; }
;                     {
;                         f32x4 sc[4];
;                         float bia[4][4];
;                         bf16x8 akq[4][2], avq[2][4];
;                         if (MODE == 3) {
; #pragma unroll
;                             for (int kt = 0; kt < 4; ++kt)
; #pragma unroll
;                                 for (int ks = 0; ks < 2; ++ks) akq[kt][ks] = *(const LAS bf16x8*)(L + LK + (16 * kt + n) * 128 + ((((4 * ks + q) ^ n) & 7) << 4));
;                             if (!far) { const LAS float* tp = biasd + hr * NT + (DOFF - tq + p0) + 4 * q;
; #pragma unroll
;                                 for (int kt = 0; kt < 4; ++kt)
; #pragma unroll
;                                     for (int r = 0; r < 4; ++r) bia[kt][r] = tp[16 * kt + r]; }
.LBB0_1241:
	s_cmp_lt_i32 s63, 0
	s_cselect_b64 s[0:1], -1, 0
	s_cmp_gt_i32 s63, s15
	s_cselect_b64 s[2:3], -1, 0
	s_or_b64 s[0:1], s[0:1], s[2:3]
	s_and_b64 vcc, exec, s[0:1]
	s_cbranch_vccnz .LBB0_1263
	s_bfe_u32 s0, s91, 0x80000
	s_cmp_eq_u32 s0, 0
	s_cbranch_scc1 .LBB0_1263
	s_sub_i32 s1, s16, s63
	s_cmpk_lt_i32 s1, 0x316
	s_cselect_b64 s[2:3], -1, 0
	s_and_b32 s1, s0, 15
	v_cndmask_b32_e64 v106, 0, 1, s[2:3]
	s_cmp_eq_u32 s1, 0
	v_add_u32_e32 v237, v206, v195
	v_add_u32_e32 v238, v206, v204
	v_add_u32_e32 v239, v208, v195
	v_add_u32_e32 v240, v208, v204
	v_add_u32_e32 v241, v209, v195
	v_add_u32_e32 v245, v209, v204
	v_add_u32_e32 v246, v210, v195
	v_add_u32_e32 v247, v210, v204
	v_cmp_ne_u32_e64 s[2:3], 1, v106
	s_cbranch_scc1 .LBB0_1254
	ds_read_b128 v[106:109], v237
	ds_read_b128 v[110:113], v238
	ds_read_b128 v[114:117], v239
	ds_read_b128 v[118:121], v240
	ds_read_b128 v[122:125], v241
	ds_read_b128 v[126:129], v245
	ds_read_b128 v[130:133], v246
	ds_read_b128 v[134:137], v247
	s_and_b64 vcc, exec, s[2:3]
	s_cbranch_vccnz .LBB0_1248
	v_sub_u32_e32 v138, s63, v196
	v_lshl_add_u32 v138, v138, 2, v233
	v_add_u32_e32 v139, 0xffc, v138
	ds_read2_b32 v[168:169], v139 offset1:1
	ds_read2_b32 v[170:171], v139 offset0:2 offset1:3
	ds_read2_b32 v[172:173], v139 offset0:16 offset1:17
	ds_read2_b32 v[174:175], v139 offset0:18 offset1:19
	ds_read2_b32 v[176:177], v139 offset0:32 offset1:33
	ds_read2_b32 v[178:179], v139 offset0:34 offset1:35
	ds_read2_b32 v[180:181], v139 offset0:48 offset1:49
	ds_read2_b32 v[182:183], v139 offset0:50 offset1:51

; #define LAS __attribute__((address_space(3)))
;     ...
;                     if (MODE == 3) { colsel = (tokmask >> (4 * qd + (n >> 2))) & 1u; if (((tokmask >> (4 * qd)) & 0xfu) == 0u) continue; }
;                     {
;                         f32x4 sc[4];
;                         float bia[4][4];
;                         bf16x8 akq[4][2], avq[2][4];
;                         if (MODE == 3) {
; #pragma unroll
;                             for (int kt = 0; kt < 4; ++kt)
; #pragma unroll
;                                 for (int ks = 0; ks < 2; ++ks) akq[kt][ks] = *(const LAS bf16x8*)(L + LK + (16 * kt + n) * 128 + ((((4 * ks + q) ^ n) & 7) << 4));
;                             if (!far) { const LAS float* tp = biasd + hr * NT + (DOFF - tq + p0) + 4 * q;
; #pragma unroll
;                                 for (int kt = 0; kt < 4; ++kt)
; #pragma unroll
;                                     for (int r = 0; r < 4; ++r) bia[kt][r] = tp[16 * kt + r]; }
.LBB0_1254:
	s_and_b32 s1, s0, 0xf0
	s_cmp_eq_u32 s1, 0
	s_cbranch_scc1 .LBB0_1263
	ds_read_b128 v[106:109], v237
	ds_read_b128 v[110:113], v238
	ds_read_b128 v[114:117], v239
	ds_read_b128 v[118:121], v240
	ds_read_b128 v[122:125], v241
	ds_read_b128 v[126:129], v245
	ds_read_b128 v[130:133], v246
	ds_read_b128 v[134:137], v247
	s_and_b64 vcc, exec, s[2:3]
	s_cbranch_vccnz .LBB0_1257
	v_sub_u32_e32 v138, s63, v184
	v_lshl_add_u32 v138, v138, 2, v233
	v_add_u32_e32 v139, 0xffc, v138
	ds_read2_b32 v[168:169], v139 offset1:1
	ds_read2_b32 v[170:171], v139 offset0:2 offset1:3
	ds_read2_b32 v[172:173], v139 offset0:16 offset1:17
	ds_read2_b32 v[174:175], v139 offset0:18 offset1:19
	ds_read2_b32 v[176:177], v139 offset0:32 offset1:33
	ds_read2_b32 v[178:179], v139 offset0:34 offset1:35
	ds_read2_b32 v[180:181], v139 offset0:48 offset1:49
	ds_read2_b32 v[182:183], v139 offset0:50 offset1:51

; #define LAS __attribute__((address_space(3)))
;     ...
;                     if (MODE == 3) { colsel = (tokmask >> (4 * qd + (n >> 2))) & 1u; if (((tokmask >> (4 * qd)) & 0xfu) == 0u) continue; }
;                     {
;                         f32x4 sc[4];
;                         float bia[4][4];
;                         bf16x8 akq[4][2], avq[2][4];
;                         if (MODE == 3) {
; #pragma unroll
;                             for (int kt = 0; kt < 4; ++kt)
; #pragma unroll
;                                 for (int ks = 0; ks < 2; ++ks) akq[kt][ks] = *(const LAS bf16x8*)(L + LK + (16 * kt + n) * 128 + ((((4 * ks + q) ^ n) & 7) << 4));
;                             if (!far) { const LAS float* tp = biasd + hr * NT + (DOFF - tq + p0) + 4 * q;
; #pragma unroll
;                                 for (int kt = 0; kt < 4; ++kt)
; #pragma unroll
;                                     for (int r = 0; r < 4; ++r) bia[kt][r] = tp[16 * kt + r]; }
.LBB0_1263:
	s_cmp_lt_i32 s53, 0
	s_cselect_b64 s[0:1], -1, 0
	s_cmp_gt_i32 s53, s15
	s_cselect_b64 s[2:3], -1, 0
	s_or_b64 s[0:1], s[0:1], s[2:3]
	s_and_b64 vcc, exec, s[0:1]
	s_cbranch_vccnz .LBB0_1285
	s_bfe_u32 s0, s91, 0x80008
	s_cmp_eq_u32 s0, 0
	s_cbranch_scc1 .LBB0_1285
	s_sub_i32 s1, s16, s53
	s_cmpk_lt_i32 s1, 0x316
	s_cselect_b64 s[2:3], -1, 0
	s_and_b32 s1, s0, 15
	v_cndmask_b32_e64 v106, 0, 1, s[2:3]
	s_cmp_eq_u32 s1, 0
	v_add_u32_e32 v237, v211, v195
	v_add_u32_e32 v238, v211, v204
	v_add_u32_e32 v239, v213, v195
	v_add_u32_e32 v240, v213, v204
	v_add_u32_e32 v241, v214, v195
	v_add_u32_e32 v245, v214, v204
	v_add_u32_e32 v246, v215, v195
	v_add_u32_e32 v247, v215, v204
	v_cmp_ne_u32_e64 s[2:3], 1, v106
	s_cbranch_scc1 .LBB0_1276
	ds_read_b128 v[106:109], v237
	ds_read_b128 v[110:113], v238
	ds_read_b128 v[114:117], v239
	ds_read_b128 v[118:121], v240
	ds_read_b128 v[122:125], v241
	ds_read_b128 v[126:129], v245
	ds_read_b128 v[130:133], v246
	ds_read_b128 v[134:137], v247
	s_and_b64 vcc, exec, s[2:3]
	s_cbranch_vccnz .LBB0_1270
	v_sub_u32_e32 v138, s53, v196
	v_lshl_add_u32 v138, v138, 2, v233
	v_add_u32_e32 v139, 0xffc, v138
	ds_read2_b32 v[168:169], v139 offset1:1
	ds_read2_b32 v[170:171], v139 offset0:2 offset1:3
	ds_read2_b32 v[172:173], v139 offset0:16 offset1:17
	ds_read2_b32 v[174:175], v139 offset0:18 offset1:19
	ds_read2_b32 v[176:177], v139 offset0:32 offset1:33
	ds_read2_b32 v[178:179], v139 offset0:34 offset1:35
	ds_read2_b32 v[180:181], v139 offset0:48 offset1:49
	ds_read2_b32 v[182:183], v139 offset0:50 offset1:51

; #define LAS __attribute__((address_space(3)))
;     ...
;                     if (MODE == 3) { colsel = (tokmask >> (4 * qd + (n >> 2))) & 1u; if (((tokmask >> (4 * qd)) & 0xfu) == 0u) continue; }
;                     {
;                         f32x4 sc[4];
;                         float bia[4][4];
;                         bf16x8 akq[4][2], avq[2][4];
;                         if (MODE == 3) {
; #pragma unroll
;                             for (int kt = 0; kt < 4; ++kt)
; #pragma unroll
;                                 for (int ks = 0; ks < 2; ++ks) akq[kt][ks] = *(const LAS bf16x8*)(L + LK + (16 * kt + n) * 128 + ((((4 * ks + q) ^ n) & 7) << 4));
;                             if (!far) { const LAS float* tp = biasd + hr * NT + (DOFF - tq + p0) + 4 * q;
; #pragma unroll
;                                 for (int kt = 0; kt < 4; ++kt)
; #pragma unroll
;                                     for (int r = 0; r < 4; ++r) bia[kt][r] = tp[16 * kt + r]; }
.LBB0_1276:
	s_and_b32 s1, s0, 0xf0
	s_cmp_eq_u32 s1, 0
	s_cbranch_scc1 .LBB0_1285
	ds_read_b128 v[106:109], v237
	ds_read_b128 v[110:113], v238
	ds_read_b128 v[114:117], v239
	ds_read_b128 v[118:121], v240
	ds_read_b128 v[122:125], v241
	ds_read_b128 v[126:129], v245
	ds_read_b128 v[130:133], v246
	ds_read_b128 v[134:137], v247
	s_and_b64 vcc, exec, s[2:3]
	s_cbranch_vccnz .LBB0_1279
	v_sub_u32_e32 v138, s53, v184
	v_lshl_add_u32 v138, v138, 2, v233
	v_add_u32_e32 v139, 0xffc, v138
	ds_read2_b32 v[168:169], v139 offset1:1
	ds_read2_b32 v[170:171], v139 offset0:2 offset1:3
	ds_read2_b32 v[172:173], v139 offset0:16 offset1:17
	ds_read2_b32 v[174:175], v139 offset0:18 offset1:19
	ds_read2_b32 v[176:177], v139 offset0:32 offset1:33
	ds_read2_b32 v[178:179], v139 offset0:34 offset1:35
	ds_read2_b32 v[180:181], v139 offset0:48 offset1:49
	ds_read2_b32 v[182:183], v139 offset0:50 offset1:51

; #define LAS __attribute__((address_space(3)))
;     ...
;                     if (MODE == 3) { colsel = (tokmask >> (4 * qd + (n >> 2))) & 1u; if (((tokmask >> (4 * qd)) & 0xfu) == 0u) continue; }
;                     {
;                         f32x4 sc[4];
;                         float bia[4][4];
;                         bf16x8 akq[4][2], avq[2][4];
;                         if (MODE == 3) {
; #pragma unroll
;                             for (int kt = 0; kt < 4; ++kt)
; #pragma unroll
;                                 for (int ks = 0; ks < 2; ++ks) akq[kt][ks] = *(const LAS bf16x8*)(L + LK + (16 * kt + n) * 128 + ((((4 * ks + q) ^ n) & 7) << 4));
;                             if (!far) { const LAS float* tp = biasd + hr * NT + (DOFF - tq + p0) + 4 * q;
; #pragma unroll
;                                 for (int kt = 0; kt < 4; ++kt)
; #pragma unroll
;                                     for (int r = 0; r < 4; ++r) bia[kt][r] = tp[16 * kt + r]; }
.LBB0_1285:
	s_cmp_lt_i32 s29, 0
	s_cselect_b64 s[0:1], -1, 0
	s_cmp_gt_i32 s29, s15
	s_cselect_b64 s[2:3], -1, 0
	s_or_b64 s[0:1], s[0:1], s[2:3]
	s_and_b64 vcc, exec, s[0:1]
	s_cbranch_vccnz .LBB0_1307
	s_bfe_u32 s0, s91, 0x80010
	s_cmp_eq_u32 s0, 0
	s_cbranch_scc1 .LBB0_1307
	s_sub_i32 s1, s16, s29
	s_cmpk_lt_i32 s1, 0x316
	s_cselect_b64 s[2:3], -1, 0
	s_and_b32 s1, s0, 15
	v_cndmask_b32_e64 v106, 0, 1, s[2:3]
	s_cmp_eq_u32 s1, 0
	v_add_u32_e32 v237, v216, v195
	v_add_u32_e32 v238, v216, v204
	v_add_u32_e32 v239, v218, v195
	v_add_u32_e32 v240, v218, v204
	v_add_u32_e32 v241, v219, v195
	v_add_u32_e32 v245, v219, v204
	v_add_u32_e32 v246, v220, v195
	v_add_u32_e32 v247, v220, v204
	v_cmp_ne_u32_e64 s[2:3], 1, v106
	s_cbranch_scc1 .LBB0_1298
	ds_read_b128 v[106:109], v237
	ds_read_b128 v[110:113], v238
	ds_read_b128 v[114:117], v239
	ds_read_b128 v[118:121], v240
	ds_read_b128 v[122:125], v241
	ds_read_b128 v[126:129], v245
	ds_read_b128 v[130:133], v246
	ds_read_b128 v[134:137], v247
	s_and_b64 vcc, exec, s[2:3]
	s_cbranch_vccnz .LBB0_1292
	v_sub_u32_e32 v138, s29, v196
	v_lshl_add_u32 v138, v138, 2, v233
	v_add_u32_e32 v139, 0xffc, v138
	ds_read2_b32 v[168:169], v139 offset1:1
	ds_read2_b32 v[170:171], v139 offset0:2 offset1:3
	ds_read2_b32 v[172:173], v139 offset0:16 offset1:17
	ds_read2_b32 v[174:175], v139 offset0:18 offset1:19
	ds_read2_b32 v[176:177], v139 offset0:32 offset1:33
	ds_read2_b32 v[178:179], v139 offset0:34 offset1:35
	ds_read2_b32 v[180:181], v139 offset0:48 offset1:49
	ds_read2_b32 v[182:183], v139 offset0:50 offset1:51

; #define LAS __attribute__((address_space(3)))
;     ...
;                     if (MODE == 3) { colsel = (tokmask >> (4 * qd + (n >> 2))) & 1u; if (((tokmask >> (4 * qd)) & 0xfu) == 0u) continue; }
;                     {
;                         f32x4 sc[4];
;                         float bia[4][4];
;                         bf16x8 akq[4][2], avq[2][4];
;                         if (MODE == 3) {
; #pragma unroll
;                             for (int kt = 0; kt < 4; ++kt)
; #pragma unroll
;                                 for (int ks = 0; ks < 2; ++ks) akq[kt][ks] = *(const LAS bf16x8*)(L + LK + (16 * kt + n) * 128 + ((((4 * ks + q) ^ n) & 7) << 4));
;                             if (!far) { const LAS float* tp = biasd + hr * NT + (DOFF - tq + p0) + 4 * q;
; #pragma unroll
;                                 for (int kt = 0; kt < 4; ++kt)
; #pragma unroll
;                                     for (int r = 0; r < 4; ++r) bia[kt][r] = tp[16 * kt + r]; }
.LBB0_1298:
	s_and_b32 s1, s0, 0xf0
	s_cmp_eq_u32 s1, 0
	s_cbranch_scc1 .LBB0_1307
	ds_read_b128 v[106:109], v237
	ds_read_b128 v[110:113], v238
	ds_read_b128 v[114:117], v239
	ds_read_b128 v[118:121], v240
	ds_read_b128 v[122:125], v241
	ds_read_b128 v[126:129], v245
	ds_read_b128 v[130:133], v246
	ds_read_b128 v[134:137], v247
	s_and_b64 vcc, exec, s[2:3]
	s_cbranch_vccnz .LBB0_1301
	v_sub_u32_e32 v138, s29, v184
	v_lshl_add_u32 v138, v138, 2, v233
	v_add_u32_e32 v139, 0xffc, v138
	ds_read2_b32 v[168:169], v139 offset1:1
	ds_read2_b32 v[170:171], v139 offset0:2 offset1:3
	ds_read2_b32 v[172:173], v139 offset0:16 offset1:17
	ds_read2_b32 v[174:175], v139 offset0:18 offset1:19
	ds_read2_b32 v[176:177], v139 offset0:32 offset1:33
	ds_read2_b32 v[178:179], v139 offset0:34 offset1:35
	ds_read2_b32 v[180:181], v139 offset0:48 offset1:49
	ds_read2_b32 v[182:183], v139 offset0:50 offset1:51
